# qkv epilogue stores nt (on top of wo nt)
# baseline (speedup 1.0000x reference)
.LBB3_3:
	v_lshl_add_u64 v[156:157], v[108:109], 0, v[96:97]
	v_readfirstlane_b32 s0, v122
	v_add_u32_e32 v160, 0x2000, v122
	v_lshl_add_u64 v[158:159], v[156:157], 0, s[18:19]
	s_mov_b32 m0, s0
	v_readfirstlane_b32 s0, v160
	v_add_u32_e32 v160, 0x4000, v122
	global_load_lds_dwordx4 v[158:159], off
	v_lshl_add_u64 v[158:159], v[156:157], 0, s[2:3]
	s_mov_b32 m0, s0
	v_readfirstlane_b32 s0, v160
	global_load_lds_dwordx4 v[158:159], off
	v_lshl_add_u64 v[158:159], v[156:157], 0, s[8:9]
	s_mov_b32 m0, s0
	v_lshl_add_u64 v[156:157], v[156:157], 0, s[10:11]
	global_load_lds_dwordx4 v[158:159], off
	v_add_u32_e32 v158, 0x6000, v122
	v_add_u32_e32 v160, 0x8000, v122
	v_readfirstlane_b32 s0, v158
	s_mov_b32 m0, s0
	v_readfirstlane_b32 s0, v160
	global_load_lds_dwordx4 v[156:157], off
	v_lshl_add_u64 v[156:157], v[106:107], 0, v[96:97]
	v_lshl_add_u64 v[158:159], v[156:157], 0, s[18:19]
	s_mov_b32 m0, s0
	v_lshl_add_u64 v[156:157], v[156:157], 0, s[2:3]
	global_load_lds_dwordx4 v[158:159], off
	v_add_u32_e32 v158, 0xa000, v122
	ds_read_b128 v[160:163], v123 offset:4096
	v_readfirstlane_b32 s0, v158
	s_mov_b32 m0, s0
	v_readfirstlane_b32 s0, v155
	global_load_lds_dwordx4 v[156:157], off
	v_lshl_add_u64 v[156:157], v[104:105], 0, v[96:97]
	s_mov_b32 m0, s0
	ds_read_b128 v[164:167], v124 offset:32768
	global_load_lds_dwordx4 v[156:157], off
	ds_read_b128 v[156:159], v123
	ds_read_b128 v[168:171], v124 offset:36864
	ds_read_b128 v[172:175], v125
	s_waitcnt lgkmcnt(0)
	v_mfma_f32_32x32x16_f16 v[80:95], v[156:159], v[164:167], v[80:95]
	ds_read_b128 v[176:179], v126
	v_mfma_f32_32x32x16_f16 v[64:79], v[156:159], v[168:171], v[64:79]
	ds_read_b128 v[180:183], v126 offset:4096
	v_mfma_f32_32x32x16_f16 v[48:63], v[160:163], v[164:167], v[48:63]
	ds_read_b128 v[164:167], v127 offset:32768
	v_mfma_f32_32x32x16_f16 v[32:47], v[160:163], v[168:171], v[32:47]
	ds_read_b128 v[168:171], v127 offset:36864
	v_mfma_f32_32x32x16_f16 v[16:31], v[172:175], v[156:159], v[16:31]
	ds_read_b128 v[156:159], v128
	s_waitcnt lgkmcnt(0)
	v_mfma_f32_32x32x16_f16 v[80:95], v[176:179], v[164:167], v[80:95]
	ds_read_b128 v[184:187], v129
	v_mfma_f32_32x32x16_f16 v[64:79], v[176:179], v[168:171], v[64:79]
	ds_read_b128 v[188:191], v129 offset:4096
	v_mfma_f32_32x32x16_f16 v[48:63], v[180:183], v[164:167], v[48:63]
	ds_read_b128 v[164:167], v130 offset:32768
	v_mfma_f32_32x32x16_f16 v[32:47], v[180:183], v[168:171], v[32:47]
	ds_read_b128 v[168:171], v130 offset:36864
	v_mfma_f32_32x32x16_f16 v[16:31], v[156:159], v[176:179], v[16:31]
	ds_read_b128 v[176:179], v131
	s_waitcnt lgkmcnt(0)
	v_mfma_f32_32x32x16_f16 v[80:95], v[184:187], v[164:167], v[80:95]
	ds_read_b128 v[192:195], v132
	v_mfma_f32_32x32x16_f16 v[64:79], v[184:187], v[168:171], v[64:79]
	ds_read_b128 v[196:199], v132 offset:4096
	v_mfma_f32_32x32x16_f16 v[48:63], v[188:191], v[164:167], v[48:63]
	ds_read_b128 v[164:167], v133 offset:32768
	v_mfma_f32_32x32x16_f16 v[32:47], v[188:191], v[168:171], v[32:47]
	ds_read_b128 v[168:171], v133 offset:36864
	v_mfma_f32_32x32x16_f16 v[16:31], v[176:179], v[184:187], v[16:31]
	ds_read_b128 v[184:187], v134
	s_add_i32 s27, s26, 2
	s_cmp_lt_u32 s26, 30
	s_cselect_b32 s0, s25, 0x7c0
	v_readfirstlane_b32 s30, v115
	s_lshl_b64 s[28:29], s[0:1], 1
	v_readfirstlane_b32 s31, v116
	v_mfma_f32_32x32x16_f16 v[0:15], v[172:175], v[160:163], v[0:15]
	v_lshl_add_u64 v[160:161], v[100:101], 0, s[28:29]
	s_mov_b32 m0, s30
	s_waitcnt vmcnt(0)
	s_waitcnt vmcnt(0) lgkmcnt(0)
	s_barrier
	v_readfirstlane_b32 s33, v117
	v_mfma_f32_32x32x16_f16 v[80:95], v[192:195], v[164:167], v[80:95]
	global_load_lds_dwordx4 v[160:161], off
	s_mov_b32 m0, s31
	v_readfirstlane_b32 s34, v118
	v_readfirstlane_b32 s35, v119
	v_readfirstlane_b32 s36, v120
	v_lshl_add_u64 v[162:163], v[98:99], 0, s[28:29]
	v_mfma_f32_32x32x16_f16 v[48:63], v[196:199], v[164:167], v[48:63]
	v_lshl_add_u64 v[166:167], v[160:161], 0, s[12:13]
	global_load_lds_dwordx4 v[166:167], off
	s_mov_b32 m0, s33
	v_readfirstlane_b32 s37, v121
	v_lshl_add_u64 v[164:165], v[102:103], 0, s[28:29]
	s_addk_i32 s25, 0x80
	v_mfma_f32_32x32x16_f16 v[64:79], v[192:195], v[168:171], v[64:79]
	s_cmp_gt_u32 s26, 29
	v_mfma_f32_32x32x16_f16 v[32:47], v[196:199], v[168:171], v[32:47]
	v_lshl_add_u64 v[168:169], v[160:161], 0, s[14:15]
	v_lshl_add_u64 v[160:161], v[160:161], 0, s[16:17]
	global_load_lds_dwordx4 v[168:169], off
	s_mov_b32 m0, s34
	v_lshl_add_u64 v[170:171], v[162:163], 0, s[12:13]
	global_load_lds_dwordx4 v[160:161], off
	s_mov_b32 m0, s35
	v_mfma_f32_32x32x16_f16 v[0:15], v[156:159], v[180:183], v[0:15]
	global_load_lds_dwordx4 v[162:163], off
	s_mov_b32 m0, s36
	ds_read_b128 v[156:159], v137
	global_load_lds_dwordx4 v[170:171], off
	s_mov_b32 m0, s37
	v_mfma_f32_32x32x16_f16 v[0:15], v[176:179], v[188:191], v[0:15]
	global_load_lds_dwordx4 v[164:165], off
	ds_read_b128 v[160:163], v138
	ds_read_b128 v[164:167], v139
	ds_read_b128 v[168:171], v135
	ds_read_b128 v[172:175], v136
	v_mfma_f32_32x32x16_f16 v[16:31], v[184:187], v[192:195], v[16:31]
	v_mfma_f32_32x32x16_f16 v[0:15], v[184:187], v[196:199], v[0:15]
	s_waitcnt lgkmcnt(0)
	v_mfma_f32_32x32x16_f16 v[80:95], v[168:171], v[156:159], v[80:95]
	ds_read_b128 v[176:179], v140
	v_mfma_f32_32x32x16_f16 v[64:79], v[168:171], v[160:163], v[64:79]
	ds_read_b128 v[180:183], v141
	v_mfma_f32_32x32x16_f16 v[48:63], v[172:175], v[156:159], v[48:63]
	ds_read_b128 v[156:159], v142
	v_mfma_f32_32x32x16_f16 v[32:47], v[172:175], v[160:163], v[32:47]
	ds_read_b128 v[160:163], v143
	v_mfma_f32_32x32x16_f16 v[16:31], v[164:167], v[168:171], v[16:31]
	ds_read_b128 v[168:171], v144
	v_mfma_f32_32x32x16_f16 v[0:15], v[164:167], v[172:175], v[0:15]
	s_waitcnt lgkmcnt(0)
	v_mfma_f32_32x32x16_f16 v[80:95], v[176:179], v[156:159], v[80:95]
	ds_read_b128 v[164:167], v145
	v_mfma_f32_32x32x16_f16 v[64:79], v[176:179], v[160:163], v[64:79]
	ds_read_b128 v[172:175], v146
	v_mfma_f32_32x32x16_f16 v[48:63], v[180:183], v[156:159], v[48:63]
	ds_read_b128 v[156:159], v147
	v_mfma_f32_32x32x16_f16 v[32:47], v[180:183], v[160:163], v[32:47]
	ds_read_b128 v[160:163], v148
	v_mfma_f32_32x32x16_f16 v[16:31], v[168:171], v[176:179], v[16:31]
	ds_read_b128 v[176:179], v149
	v_mfma_f32_32x32x16_f16 v[0:15], v[168:171], v[180:183], v[0:15]
	s_waitcnt lgkmcnt(0)
	v_mfma_f32_32x32x16_f16 v[80:95], v[164:167], v[156:159], v[80:95]
	ds_read_b128 v[168:171], v150
	v_mfma_f32_32x32x16_f16 v[64:79], v[164:167], v[160:163], v[64:79]
	ds_read_b128 v[180:183], v151
	v_mfma_f32_32x32x16_f16 v[48:63], v[172:175], v[156:159], v[48:63]
	ds_read_b128 v[156:159], v152
	v_mfma_f32_32x32x16_f16 v[32:47], v[172:175], v[160:163], v[32:47]
	ds_read_b128 v[160:163], v153
	v_mfma_f32_32x32x16_f16 v[16:31], v[176:179], v[164:167], v[16:31]
	ds_read_b128 v[164:167], v154
	v_mfma_f32_32x32x16_f16 v[0:15], v[176:179], v[172:175], v[0:15]
	s_waitcnt lgkmcnt(0)
	v_mfma_f32_32x32x16_f16 v[80:95], v[168:171], v[156:159], v[80:95]
	s_waitcnt vmcnt(0)
	v_lshl_add_u64 v[104:105], v[104:105], 0, s[20:21]
	v_lshl_add_u64 v[106:107], v[106:107], 0, s[20:21]
	v_lshl_add_u64 v[108:109], v[108:109], 0, s[20:21]
	s_mov_b32 s26, s27
	s_waitcnt vmcnt(0)
	s_barrier
	v_mfma_f32_32x32x16_f16 v[64:79], v[168:171], v[160:163], v[64:79]
	v_mfma_f32_32x32x16_f16 v[48:63], v[180:183], v[156:159], v[48:63]
	v_mfma_f32_32x32x16_f16 v[32:47], v[180:183], v[160:163], v[32:47]
	v_mfma_f32_32x32x16_f16 v[16:31], v[164:167], v[168:171], v[16:31]
	v_mfma_f32_32x32x16_f16 v[0:15], v[164:167], v[180:183], v[0:15]
	s_cbranch_scc0 .LBB3_3
	v_lshlrev_b32_e32 v96, 1, v112
	v_lshl_or_b32 v96, s23, 2, v96
	v_ashrrev_i32_e32 v97, 31, v96
	v_add_u32_e32 v102, s24, v114
	v_lshlrev_b32_e32 v103, 2, v113
	v_lshlrev_b64 v[96:97], 18, v[96:97]
	v_lshl_add_u64 v[96:97], s[4:5], 0, v[96:97]
	v_or_b32_e32 v100, v102, v103
	v_lshlrev_b32_e32 v98, 1, v110
	v_mov_b32_e32 v99, 0
	v_lshl_add_u64 v[96:97], v[96:97], 0, v[98:99]
	s_mov_b32 s0, 0x38800000
	s_cmp_lt_u32 s23, 16
	s_cselect_b32 s0, 0x38b8aa3b, s0
	v_lshlrev_b32_e32 v98, 7, v100
	v_lshl_add_u64 v[100:101], v[96:97], 0, v[98:99]
	v_fma_mixlo_f16 v64, v64, s0, 0
	global_store_short v[100:101], v64, off offset:64 nt
	v_fma_mixlo_f16 v64, v65, s0, 0
	global_store_short v[100:101], v64, off offset:192 nt
	v_fma_mixlo_f16 v64, v66, s0, 0
	global_store_short v[100:101], v64, off offset:320 nt
	v_fma_mixlo_f16 v64, v67, s0, 0
	global_store_short v[100:101], v64, off offset:448 nt
	v_fma_mixlo_f16 v64, v68, s0, 0
	global_store_short v[100:101], v64, off offset:1088 nt
	v_fma_mixlo_f16 v64, v69, s0, 0
	global_store_short v[100:101], v64, off offset:1216 nt
	v_fma_mixlo_f16 v64, v70, s0, 0
	global_store_short v[100:101], v64, off offset:1344 nt
	v_fma_mixlo_f16 v64, v71, s0, 0
	global_store_short v[100:101], v64, off offset:1472 nt
	v_fma_mixlo_f16 v64, v72, s0, 0
	global_store_short v[100:101], v64, off offset:2112 nt
	v_fma_mixlo_f16 v64, v73, s0, 0
	global_store_short v[100:101], v64, off offset:2240 nt
	v_fma_mixlo_f16 v64, v74, s0, 0
	global_store_short v[100:101], v64, off offset:2368 nt
	v_fma_mixlo_f16 v64, v75, s0, 0
	global_store_short v[100:101], v64, off offset:2496 nt
	v_fma_mixlo_f16 v64, v76, s0, 0
	global_store_short v[100:101], v64, off offset:3136 nt
	v_fma_mixlo_f16 v64, v77, s0, 0
	global_store_short v[100:101], v64, off offset:3264 nt
	v_fma_mixlo_f16 v64, v78, s0, 0
	global_store_short v[100:101], v64, off offset:3392 nt
	v_fma_mixlo_f16 v64, v79, s0, 0
	global_store_short v[100:101], v64, off offset:3520 nt
	v_or_b32_e32 v64, 0x1000, v98
	v_mov_b32_e32 v65, v99
	v_fma_mixlo_f16 v48, v48, s0, 0
	v_lshl_add_u64 v[66:67], v[96:97], 0, v[64:65]
	global_store_short v[66:67], v48, off nt
	v_fma_mixlo_f16 v68, v49, s0, 0
	v_or_b32_e32 v48, 0x1080, v98
	v_mov_b32_e32 v49, v99
	v_lshl_add_u64 v[66:67], v[96:97], 0, v[48:49]
	global_store_short v[66:67], v68, off nt
	v_or_b32_e32 v66, 0x1100, v98
	v_mov_b32_e32 v67, v99
	v_fma_mixlo_f16 v50, v50, s0, 0
	v_lshl_add_u64 v[68:69], v[96:97], 0, v[66:67]
	global_store_short v[68:69], v50, off nt
	v_fma_mixlo_f16 v70, v51, s0, 0
	v_or_b32_e32 v50, 0x1180, v98
	v_mov_b32_e32 v51, v99
	v_lshl_add_u64 v[68:69], v[96:97], 0, v[50:51]
	global_store_short v[68:69], v70, off nt
	v_or_b32_e32 v68, 0x1400, v98
	v_mov_b32_e32 v69, v99
	v_fma_mixlo_f16 v52, v52, s0, 0
	v_lshl_add_u64 v[70:71], v[96:97], 0, v[68:69]
	global_store_short v[70:71], v52, off nt
	v_fma_mixlo_f16 v72, v53, s0, 0
	v_or_b32_e32 v52, 0x1480, v98
	v_mov_b32_e32 v53, v99
	v_lshl_add_u64 v[70:71], v[96:97], 0, v[52:53]
	global_store_short v[70:71], v72, off nt
	v_or_b32_e32 v70, 0x1500, v98
	v_mov_b32_e32 v71, v99
	v_fma_mixlo_f16 v54, v54, s0, 0
	v_lshl_add_u64 v[72:73], v[96:97], 0, v[70:71]
	v_fma_mixlo_f16 v80, v80, s0, 0
	global_store_short v[72:73], v54, off nt
	v_fma_mixlo_f16 v74, v55, s0, 0
	v_or_b32_e32 v54, 0x1580, v98
	v_mov_b32_e32 v55, v99
	global_store_short v[100:101], v80, off nt
	v_fma_mixlo_f16 v80, v81, s0, 0
	v_lshl_add_u64 v[72:73], v[96:97], 0, v[54:55]
	global_store_short v[100:101], v80, off offset:128 nt
	v_fma_mixlo_f16 v80, v82, s0, 0
	global_store_short v[72:73], v74, off nt
	v_or_b32_e32 v72, 0x1800, v98
	v_mov_b32_e32 v73, v99
	global_store_short v[100:101], v80, off offset:256 nt
	v_fma_mixlo_f16 v80, v83, s0, 0
	v_fma_mixlo_f16 v56, v56, s0, 0
	v_lshl_add_u64 v[74:75], v[96:97], 0, v[72:73]
	global_store_short v[100:101], v80, off offset:384 nt
	v_fma_mixlo_f16 v80, v84, s0, 0
	global_store_short v[74:75], v56, off nt
	v_fma_mixlo_f16 v76, v57, s0, 0
	v_or_b32_e32 v56, 0x1880, v98
	v_mov_b32_e32 v57, v99
	global_store_short v[100:101], v80, off offset:1024 nt
	v_fma_mixlo_f16 v80, v85, s0, 0
	v_lshl_add_u64 v[74:75], v[96:97], 0, v[56:57]
	global_store_short v[100:101], v80, off offset:1152 nt
	v_fma_mixlo_f16 v80, v86, s0, 0
	global_store_short v[74:75], v76, off nt
	v_or_b32_e32 v74, 0x1900, v98
	v_mov_b32_e32 v75, v99
	global_store_short v[100:101], v80, off offset:1280 nt
	v_fma_mixlo_f16 v80, v87, s0, 0
	v_fma_mixlo_f16 v58, v58, s0, 0
	v_lshl_add_u64 v[76:77], v[96:97], 0, v[74:75]
	global_store_short v[100:101], v80, off offset:1408 nt
	v_fma_mixlo_f16 v80, v88, s0, 0
	global_store_short v[76:77], v58, off nt
	v_fma_mixlo_f16 v78, v59, s0, 0
	v_or_b32_e32 v58, 0x1980, v98
	v_mov_b32_e32 v59, v99
	global_store_short v[100:101], v80, off offset:2048 nt
	v_fma_mixlo_f16 v80, v89, s0, 0
	v_lshl_add_u64 v[76:77], v[96:97], 0, v[58:59]
	global_store_short v[100:101], v80, off offset:2176 nt
	v_fma_mixlo_f16 v80, v90, s0, 0
	global_store_short v[76:77], v78, off nt
	v_or_b32_e32 v76, 0x1c00, v98
	v_mov_b32_e32 v77, v99
	global_store_short v[100:101], v80, off offset:2304 nt
	v_fma_mixlo_f16 v80, v91, s0, 0
	v_fma_mixlo_f16 v60, v60, s0, 0
	v_lshl_add_u64 v[78:79], v[96:97], 0, v[76:77]
	global_store_short v[100:101], v80, off offset:2432 nt
	v_fma_mixlo_f16 v80, v92, s0, 0
	global_store_short v[78:79], v60, off nt
	v_fma_mixlo_f16 v82, v61, s0, 0
	v_or_b32_e32 v60, 0x1c80, v98
	v_mov_b32_e32 v61, v99
	global_store_short v[100:101], v80, off offset:3072 nt
	v_fma_mixlo_f16 v80, v93, s0, 0
	v_lshl_add_u64 v[78:79], v[96:97], 0, v[60:61]
	global_store_short v[100:101], v80, off offset:3200 nt
	v_fma_mixlo_f16 v80, v94, s0, 0
	global_store_short v[78:79], v82, off nt
	v_or_b32_e32 v78, 0x1d00, v98
	v_mov_b32_e32 v79, v99
	global_store_short v[100:101], v80, off offset:3328 nt
	v_fma_mixlo_f16 v80, v95, s0, 0
	v_fma_mixlo_f16 v62, v62, s0, 0
	v_lshl_add_u64 v[82:83], v[96:97], 0, v[78:79]
	v_or_b32_e32 v98, 0x1d80, v98
	global_store_short v[100:101], v80, off offset:3456 nt
	v_lshl_add_u64 v[80:81], v[96:97], 0, 64
	global_store_short v[82:83], v62, off nt
	v_fma_mixlo_f16 v82, v63, s0, 0
	v_lshl_add_u64 v[62:63], v[96:97], 0, v[98:99]
	global_store_short v[62:63], v82, off nt
	v_fma_mixlo_f16 v32, v32, s0, 0
	v_lshl_add_u64 v[62:63], v[80:81], 0, v[64:65]
	global_store_short v[62:63], v32, off nt
	v_fma_mixlo_f16 v62, v33, s0, 0
	v_lshl_add_u64 v[32:33], v[80:81], 0, v[48:49]
	global_store_short v[32:33], v62, off nt
	v_fma_mixlo_f16 v34, v34, s0, 0
	v_lshl_add_u64 v[32:33], v[80:81], 0, v[66:67]
	global_store_short v[32:33], v34, off nt
	v_fma_mixlo_f16 v34, v35, s0, 0
	v_lshl_add_u64 v[32:33], v[80:81], 0, v[50:51]
	global_store_short v[32:33], v34, off nt
	v_fma_mixlo_f16 v34, v36, s0, 0
	v_lshl_add_u64 v[32:33], v[80:81], 0, v[68:69]
	global_store_short v[32:33], v34, off nt
	v_fma_mixlo_f16 v34, v37, s0, 0
	v_lshl_add_u64 v[32:33], v[80:81], 0, v[52:53]
	global_store_short v[32:33], v34, off nt
	v_fma_mixlo_f16 v34, v38, s0, 0
	v_lshl_add_u64 v[32:33], v[80:81], 0, v[70:71]
	global_store_short v[32:33], v34, off nt
	v_fma_mixlo_f16 v34, v39, s0, 0
	v_lshl_add_u64 v[32:33], v[80:81], 0, v[54:55]
	global_store_short v[32:33], v34, off nt
	v_fma_mixlo_f16 v34, v40, s0, 0
	v_lshl_add_u64 v[32:33], v[80:81], 0, v[72:73]
	global_store_short v[32:33], v34, off nt
	v_fma_mixlo_f16 v34, v41, s0, 0
	v_lshl_add_u64 v[32:33], v[80:81], 0, v[56:57]
	global_store_short v[32:33], v34, off nt
	v_fma_mixlo_f16 v34, v42, s0, 0
	v_lshl_add_u64 v[32:33], v[80:81], 0, v[74:75]
	global_store_short v[32:33], v34, off nt
	v_fma_mixlo_f16 v34, v43, s0, 0
	v_lshl_add_u64 v[32:33], v[80:81], 0, v[58:59]
	global_store_short v[32:33], v34, off nt
	v_fma_mixlo_f16 v34, v44, s0, 0
	v_lshl_add_u64 v[32:33], v[80:81], 0, v[76:77]
	global_store_short v[32:33], v34, off nt
	v_fma_mixlo_f16 v34, v45, s0, 0
	v_lshl_add_u64 v[32:33], v[80:81], 0, v[60:61]
	global_store_short v[32:33], v34, off nt
	v_fma_mixlo_f16 v34, v46, s0, 0
	v_lshl_add_u64 v[32:33], v[80:81], 0, v[78:79]
	global_store_short v[32:33], v34, off nt
	v_fma_mixlo_f16 v34, v47, s0, 0
	v_lshl_add_u64 v[32:33], v[80:81], 0, v[98:99]
	global_store_short v[32:33], v34, off nt
	v_or3_b32 v32, v103, v111, s22
	v_or_b32_e32 v33, v102, v110
	v_lshlrev_b32_e32 v98, 1, v33
	v_ashrrev_i32_e32 v33, 31, v32
	v_lshl_add_u64 v[34:35], s[6:7], 0, v[98:99]
	s_mov_b32 s0, 0x38800000
	v_lshlrev_b64 v[36:37], 12, v[32:33]
	v_fma_mixlo_f16 v16, v16, s0, 0
	v_lshl_add_u64 v[36:37], v[34:35], 0, v[36:37]
	v_or_b32_e32 v38, 2, v32
	global_store_short v[36:37], v16, off nt
	v_or_b32_e32 v16, 1, v32
	v_ashrrev_i32_e32 v39, 31, v38
	v_fma_mixlo_f16 v33, v17, s0, 0
	v_ashrrev_i32_e32 v17, 31, v16
	v_lshlrev_b64 v[38:39], 12, v[38:39]
	v_lshlrev_b64 v[16:17], 12, v[16:17]
	v_fma_mixlo_f16 v18, v18, s0, 0
	v_lshl_add_u64 v[38:39], v[34:35], 0, v[38:39]
	v_or_b32_e32 v40, 8, v32
	v_lshl_add_u64 v[16:17], v[34:35], 0, v[16:17]
	global_store_short v[38:39], v18, off nt
	v_or_b32_e32 v18, 3, v32
	v_ashrrev_i32_e32 v41, 31, v40
	global_store_short v[16:17], v33, off nt
	v_fma_mixlo_f16 v33, v19, s0, 0
	v_ashrrev_i32_e32 v19, 31, v18
	v_lshlrev_b64 v[40:41], 12, v[40:41]
	v_lshlrev_b64 v[18:19], 12, v[18:19]
	v_fma_mixlo_f16 v20, v20, s0, 0
	v_lshl_add_u64 v[40:41], v[34:35], 0, v[40:41]
	v_or_b32_e32 v42, 10, v32
	v_lshl_add_u64 v[18:19], v[34:35], 0, v[18:19]
	global_store_short v[40:41], v20, off nt
	v_or_b32_e32 v20, 9, v32
	v_ashrrev_i32_e32 v43, 31, v42
	global_store_short v[18:19], v33, off nt
	v_fma_mixlo_f16 v33, v21, s0, 0
	v_ashrrev_i32_e32 v21, 31, v20
	v_lshlrev_b64 v[42:43], 12, v[42:43]
	v_lshlrev_b64 v[20:21], 12, v[20:21]
	v_fma_mixlo_f16 v22, v22, s0, 0
	v_lshl_add_u64 v[42:43], v[34:35], 0, v[42:43]
	v_or_b32_e32 v44, 16, v32
	v_fma_mixlo_f16 v0, v0, s0, 0
	v_lshl_add_u64 v[20:21], v[34:35], 0, v[20:21]
	global_store_short v[42:43], v22, off nt
	v_or_b32_e32 v22, 11, v32
	v_ashrrev_i32_e32 v45, 31, v44
	global_store_short v[36:37], v0, off offset:64 nt
	v_fma_mixlo_f16 v0, v1, s0, 0
	global_store_short v[20:21], v33, off nt
	v_fma_mixlo_f16 v33, v23, s0, 0
	v_ashrrev_i32_e32 v23, 31, v22
	v_lshlrev_b64 v[44:45], 12, v[44:45]
	global_store_short v[16:17], v0, off offset:64 nt
	v_fma_mixlo_f16 v0, v2, s0, 0
	v_lshlrev_b64 v[22:23], 12, v[22:23]
	v_fma_mixlo_f16 v24, v24, s0, 0
	v_lshl_add_u64 v[44:45], v[34:35], 0, v[44:45]
	v_or_b32_e32 v46, 18, v32
	global_store_short v[38:39], v0, off offset:64 nt
	v_fma_mixlo_f16 v0, v3, s0, 0
	v_lshl_add_u64 v[22:23], v[34:35], 0, v[22:23]
	global_store_short v[44:45], v24, off nt
	v_or_b32_e32 v24, 17, v32
	v_ashrrev_i32_e32 v47, 31, v46
	global_store_short v[18:19], v0, off offset:64 nt
	v_fma_mixlo_f16 v0, v4, s0, 0
	global_store_short v[22:23], v33, off nt
	v_fma_mixlo_f16 v33, v25, s0, 0
	v_ashrrev_i32_e32 v25, 31, v24
	v_lshlrev_b64 v[46:47], 12, v[46:47]
	global_store_short v[40:41], v0, off offset:64 nt
	v_fma_mixlo_f16 v0, v5, s0, 0
	v_lshlrev_b64 v[24:25], 12, v[24:25]
	v_fma_mixlo_f16 v26, v26, s0, 0
	v_lshl_add_u64 v[46:47], v[34:35], 0, v[46:47]
	v_or_b32_e32 v48, 24, v32
	global_store_short v[20:21], v0, off offset:64 nt
	v_fma_mixlo_f16 v0, v6, s0, 0
	v_lshl_add_u64 v[24:25], v[34:35], 0, v[24:25]
	global_store_short v[46:47], v26, off nt
	v_or_b32_e32 v26, 19, v32
	v_ashrrev_i32_e32 v49, 31, v48
	global_store_short v[42:43], v0, off offset:64 nt
	v_fma_mixlo_f16 v0, v7, s0, 0
	global_store_short v[24:25], v33, off nt
	v_fma_mixlo_f16 v33, v27, s0, 0
	v_ashrrev_i32_e32 v27, 31, v26
	v_lshlrev_b64 v[48:49], 12, v[48:49]
	v_or_b32_e32 v50, 26, v32
	global_store_short v[22:23], v0, off offset:64 nt
	v_fma_mixlo_f16 v0, v8, s0, 0
	v_lshlrev_b64 v[26:27], 12, v[26:27]
	v_fma_mixlo_f16 v28, v28, s0, 0
	v_lshl_add_u64 v[48:49], v[34:35], 0, v[48:49]
	v_ashrrev_i32_e32 v51, 31, v50
	global_store_short v[44:45], v0, off offset:64 nt
	v_fma_mixlo_f16 v0, v9, s0, 0
	v_lshl_add_u64 v[26:27], v[34:35], 0, v[26:27]
	global_store_short v[48:49], v28, off nt
	v_or_b32_e32 v28, 25, v32
	v_lshlrev_b64 v[50:51], 12, v[50:51]
	global_store_short v[24:25], v0, off offset:64 nt
	v_fma_mixlo_f16 v0, v10, s0, 0
	global_store_short v[26:27], v33, off nt
	v_fma_mixlo_f16 v33, v29, s0, 0
	v_ashrrev_i32_e32 v29, 31, v28
	v_fma_mixlo_f16 v30, v30, s0, 0
	v_lshl_add_u64 v[50:51], v[34:35], 0, v[50:51]
	global_store_short v[46:47], v0, off offset:64 nt
	v_fma_mixlo_f16 v0, v11, s0, 0
	v_lshlrev_b64 v[28:29], 12, v[28:29]
	global_store_short v[50:51], v30, off nt
	v_or_b32_e32 v30, 27, v32
	global_store_short v[26:27], v0, off offset:64 nt
	v_fma_mixlo_f16 v0, v12, s0, 0
	v_lshl_add_u64 v[28:29], v[34:35], 0, v[28:29]
	v_fma_mixlo_f16 v32, v31, s0, 0
	v_ashrrev_i32_e32 v31, 31, v30
	global_store_short v[48:49], v0, off offset:64 nt
	v_fma_mixlo_f16 v0, v13, s0, 0
	v_lshlrev_b64 v[30:31], 12, v[30:31]
	global_store_short v[28:29], v0, off offset:64 nt
	v_fma_mixlo_f16 v0, v14, s0, 0
	v_lshl_add_u64 v[30:31], v[34:35], 0, v[30:31]
	global_store_short v[50:51], v0, off offset:64 nt
	v_fma_mixlo_f16 v0, v15, s0, 0
	global_store_short v[28:29], v33, off nt
	global_store_short v[30:31], v32, off nt
	global_store_short v[30:31], v0, off offset:64 nt
	s_endpgm
